# v59 + DSA attention units: static priority raise (s_setprio 2) for waves 4-7, the second wave of each SIMD
# baseline (speedup 1.0000x reference)
.LBB0_1072:
	s_and_b64 s[38:39], s[52:53], exec
	v_readfirstlane_b32 s41, v235
	s_cselect_b32 s40, s92, s93
	s_ashr_i32 s31, s41, 6
	s_bitcmp1_b32 s31, 2
	s_cbranch_scc0 .Ldsa_prio_skip
	s_setprio 2
.Ldsa_prio_skip:
	s_lshl_b32 s42, s40, 8
	s_lshl_b32 s43, s31, 5
	s_or_b32 s29, s16, s42
	s_ashr_i32 s39, s43, 31
	s_add_u32 s38, s29, s43
	s_addc_u32 s39, s17, s39
	s_lshl_b64 s[38:39], s[38:39], 10
	s_add_u32 s50, s94, s38
	s_addc_u32 s51, s95, s39
	s_lshl_b32 s38, s31, 3
	s_lshl_b32 s29, s31, 4
	s_ashr_i32 s39, s38, 31
	v_and_or_b32 v0, s29, 48, v237
	s_ashr_i32 s29, s41, 3
	v_lshl_add_u64 v[216:217], s[38:39], 1, v[214:215]
	v_lshlrev_b32_e32 v0, 10, v0
	s_and_b32 s38, s29, 0xffffffe0
	v_lshl_add_u64 v[2:3], s[44:45], 0, v[0:1]
	s_ashr_i32 s39, s38, 31
	v_lshl_add_u64 v[2:3], s[38:39], 1, v[2:3]
	v_mov_b32_e32 v203, v1
	s_lshl_b32 s63, s31, 10
	s_mov_b32 s29, m0
	s_mov_b32 m0, s63
	s_nop 0
	global_load_lds_dwordx4 v[216:217], off
	s_mov_b32 m0, s29
	v_lshl_add_u64 v[218:219], v[2:3], 0, v[202:203]
	s_add_i32 s62, s63, 0x6000
	s_mov_b32 s29, m0
	s_mov_b32 m0, s62
	s_nop 0
	global_load_lds_dwordx4 v[218:219], off
	s_mov_b32 m0, s29
	v_lshl_add_u64 v[2:3], v[216:217], 0, s[12:13]
	s_add_i32 s29, s63, 0x2000
	s_mov_b32 s38, m0
	s_mov_b32 m0, s29
	s_nop 0
	global_load_lds_dwordx4 v[2:3], off
	s_mov_b32 m0, s38
	global_load_dwordx4 v[124:127], v247, s[50:51]
	global_load_dwordx4 v[120:123], v247, s[50:51] offset:32
	global_load_dwordx4 v[116:119], v247, s[50:51] offset:64
	global_load_dwordx4 v[112:115], v247, s[50:51] offset:96
	s_add_i32 s43, s43, s42
	v_or_b32_e32 v34, s43, v236
	v_ashrrev_i32_e32 v35, 31, v34
	v_lshl_add_u64 v[2:3], v[34:35], 2, s[0:1]
	v_add_co_u32_e32 v4, vcc, s10, v2
	global_load_dword v0, v[2:3], off
	s_nop 0
	v_addc_co_u32_e32 v5, vcc, 0, v3, vcc
	global_load_dword v36, v[4:5], off
	v_mov_b32_e32 v180, v1
	s_add_i32 s29, s63, 0x4000
	v_ashrrev_i32_e32 v181, 31, v180
	s_mov_b32 s57, 0
	s_waitcnt vmcnt(5)
	v_and_b32_e32 v5, 0xffff0000, v124
	v_lshlrev_b32_e32 v4, 16, v124
	v_mul_f32_e32 v6, v5, v5
	v_fmac_f32_e32 v6, v4, v4
	v_lshlrev_b32_e32 v4, 16, v125
	v_fmac_f32_e32 v6, v4, v4
	v_and_b32_e32 v4, 0xffff0000, v125
	v_fmac_f32_e32 v6, v4, v4
	v_lshlrev_b32_e32 v4, 16, v126
	v_fmac_f32_e32 v6, v4, v4
	v_and_b32_e32 v4, 0xffff0000, v126
	v_fmac_f32_e32 v6, v4, v4
	v_lshlrev_b32_e32 v4, 16, v127
	v_fmac_f32_e32 v6, v4, v4
	v_and_b32_e32 v4, 0xffff0000, v127
	v_fmac_f32_e32 v6, v4, v4
	s_waitcnt vmcnt(4)
	v_lshlrev_b32_e32 v4, 16, v120
	v_fmac_f32_e32 v6, v4, v4
	v_and_b32_e32 v4, 0xffff0000, v120
	v_fmac_f32_e32 v6, v4, v4
	v_lshlrev_b32_e32 v4, 16, v121
	v_fmac_f32_e32 v6, v4, v4
	v_and_b32_e32 v4, 0xffff0000, v121
	v_fmac_f32_e32 v6, v4, v4
	v_lshlrev_b32_e32 v4, 16, v122
	v_fmac_f32_e32 v6, v4, v4
	v_and_b32_e32 v4, 0xffff0000, v122
	v_fmac_f32_e32 v6, v4, v4
	v_lshlrev_b32_e32 v4, 16, v123
	v_fmac_f32_e32 v6, v4, v4
	v_and_b32_e32 v4, 0xffff0000, v123
	v_fmac_f32_e32 v6, v4, v4
	s_waitcnt vmcnt(3)
	v_lshlrev_b32_e32 v4, 16, v116
	v_fmac_f32_e32 v6, v4, v4
	v_and_b32_e32 v4, 0xffff0000, v116
	v_fmac_f32_e32 v6, v4, v4
	v_lshlrev_b32_e32 v4, 16, v117
	v_fmac_f32_e32 v6, v4, v4
	v_and_b32_e32 v4, 0xffff0000, v117
	v_fmac_f32_e32 v6, v4, v4
	v_lshlrev_b32_e32 v4, 16, v118
	v_fmac_f32_e32 v6, v4, v4
	v_and_b32_e32 v4, 0xffff0000, v118
	v_fmac_f32_e32 v6, v4, v4
	v_lshlrev_b32_e32 v4, 16, v119
	v_fmac_f32_e32 v6, v4, v4
	v_and_b32_e32 v4, 0xffff0000, v119
	v_fmac_f32_e32 v6, v4, v4
	s_waitcnt vmcnt(2)
	v_lshlrev_b32_e32 v4, 16, v112
	v_fmac_f32_e32 v6, v4, v4
	v_and_b32_e32 v4, 0xffff0000, v112
	v_fmac_f32_e32 v6, v4, v4
	v_lshlrev_b32_e32 v4, 16, v113
	v_fmac_f32_e32 v6, v4, v4
	v_and_b32_e32 v4, 0xffff0000, v113
	v_fmac_f32_e32 v6, v4, v4
	v_and_b32_e32 v5, 0xffff0000, v114
	v_lshlrev_b32_e32 v4, 16, v114
	v_pk_mul_f32 v[4:5], v[4:5], v[4:5]
	s_nop 0
	v_add_f32_e32 v4, v4, v6
	v_add_f32_e32 v6, v5, v4
	v_and_b32_e32 v5, 0xffff0000, v115
	v_lshlrev_b32_e32 v4, 16, v115
	v_pk_mul_f32 v[4:5], v[4:5], v[4:5]
	s_nop 0
	v_add_f32_e32 v4, v4, v6
	v_add_f32_e32 v4, v5, v4
	v_mov_b32_e32 v5, v4
	s_nop 1
	v_permlane32_swap_b32_e32 v4, v5
	v_add_f32_e32 v4, v4, v5
	v_cmp_gt_f32_e32 vcc, s7, v4
	v_mul_f32_e32 v5, 0x4f800000, v4
	s_nop 0
	v_cndmask_b32_e32 v4, v4, v5, vcc
	v_sqrt_f32_e32 v5, v4
	s_nop 0
	v_add_u32_e32 v6, -1, v5
	v_fma_f32 v7, -v6, v5, v4
	v_cmp_ge_f32_e64 s[38:39], 0, v7
	v_add_u32_e32 v7, 1, v5
	s_nop 0
	v_cndmask_b32_e64 v6, v5, v6, s[38:39]
	v_fma_f32 v5, -v7, v5, v4
	v_cmp_lt_f32_e64 s[38:39], 0, v5
	s_nop 1
	v_cndmask_b32_e64 v5, v6, v7, s[38:39]
	v_mul_f32_e32 v6, 0x37800000, v5
	v_cndmask_b32_e32 v5, v5, v6, vcc
	v_cmp_class_f32_e32 vcc, v4, v199
	v_lshl_add_u64 v[6:7], v[216:217], 0, s[24:25]
	s_nop 0
	v_cndmask_b32_e32 v4, v5, v4, vcc
	v_mul_f32_e32 v201, 0x3f8147ae, v4
	v_lshl_add_u64 v[4:5], v[180:181], 2, s[14:15]
	global_load_dword v8, v[4:5], off
	s_mov_b32 s38, m0
	s_mov_b32 m0, s29
	s_nop 0
	global_load_lds_dwordx4 v[6:7], off
	s_mov_b32 m0, s38
	s_mov_b32 s29, 0x10000
	v_add_co_u32_e32 v6, vcc, s29, v2
	s_mov_b32 s29, 0x18000
	s_nop 0
	v_addc_co_u32_e32 v7, vcc, 0, v3, vcc
	v_add_co_u32_e32 v2, vcc, s29, v2
	s_waitcnt vmcnt(3) lgkmcnt(0)
	s_barrier
	global_load_dword v211, v[6:7], off
	s_nop 0
	v_addc_co_u32_e32 v3, vcc, 0, v3, vcc
	global_load_dword v213, v[2:3], off
	global_load_dword v209, v[4:5], off offset:4
	s_waitcnt vmcnt(3)
	v_mul_f32_e32 v2, v8, v201
	v_cmp_nge_f32_e32 vcc, s73, v2
	ds_read_b128 v[18:21], v241 offset:512
	ds_read_b128 v[2:5], v241
	s_waitcnt lgkmcnt(0)
	v_mfma_f32_32x32x16_bf16 v[2:17], v[2:5], v[124:127], 0
	ds_read_b128 v[38:41], v241 offset:2560
	ds_read_b128 v[42:45], v241 offset:2048
	v_mfma_f32_32x32x16_bf16 v[18:33], v[18:21], v[124:127], 0
	s_waitcnt lgkmcnt(0)
	v_mfma_f32_32x32x16_bf16 v[2:17], v[42:45], v[120:123], v[2:17]
	v_mfma_f32_32x32x16_bf16 v[18:33], v[38:41], v[120:123], v[18:33]
	ds_read_b128 v[38:41], v241 offset:4608
	ds_read_b128 v[42:45], v241 offset:4096
	s_waitcnt lgkmcnt(0)
	v_mfma_f32_32x32x16_bf16 v[2:17], v[42:45], v[116:119], v[2:17]
	v_mfma_f32_32x32x16_bf16 v[18:33], v[38:41], v[116:119], v[18:33]
	ds_read_b128 v[38:41], v241 offset:6656
	ds_read_b128 v[42:45], v241 offset:6144
	s_waitcnt lgkmcnt(0)
	v_mfma_f32_32x32x16_bf16 v[2:17], v[42:45], v[112:115], v[2:17]
	v_mfma_f32_32x32x16_bf16 v[18:33], v[38:41], v[112:115], v[18:33]
	v_lshrrev_b32_e32 v38, v238, v0
	v_lshrrev_b32_e32 v39, v238, v36
	s_nop 15
	s_nop 7
	v_bfe_i32 v37, v38, 0, 1
	v_bfe_i32 v40, v39, 0, 1
	s_nop 6
	v_bitop3_b32 v37, v2, s6, v37 bitop3:0xe4
	v_bitop3_b32 v2, v18, s6, v40 bitop3:0xe4
	v_bfe_i32 v18, v38, 1, 1
	v_bfe_i32 v40, v39, 1, 1
	v_bitop3_b32 v18, v3, s6, v18 bitop3:0xe4
	v_bitop3_b32 v3, v19, s6, v40 bitop3:0xe4
	v_bfe_i32 v19, v38, 2, 1
	v_bfe_i32 v40, v39, 2, 1
	v_bitop3_b32 v19, v4, s6, v19 bitop3:0xe4
	v_bitop3_b32 v4, v20, s6, v40 bitop3:0xe4
	v_bfe_i32 v20, v38, 3, 1
	v_bfe_i32 v40, v39, 3, 1
	v_bitop3_b32 v20, v5, s6, v20 bitop3:0xe4
	v_bitop3_b32 v5, v21, s6, v40 bitop3:0xe4
	v_bfe_i32 v21, v38, 8, 1
	v_bfe_i32 v40, v39, 8, 1
	v_bitop3_b32 v21, v6, s6, v21 bitop3:0xe4
	v_bitop3_b32 v6, v22, s6, v40 bitop3:0xe4
	v_bfe_i32 v22, v38, 9, 1
	v_bfe_i32 v40, v39, 9, 1
	v_bitop3_b32 v22, v7, s6, v22 bitop3:0xe4
	v_bitop3_b32 v7, v23, s6, v40 bitop3:0xe4
	v_bfe_i32 v23, v38, 10, 1
	v_bfe_i32 v40, v39, 10, 1
	v_bitop3_b32 v23, v8, s6, v23 bitop3:0xe4
	v_bitop3_b32 v8, v24, s6, v40 bitop3:0xe4
	v_bfe_i32 v24, v38, 11, 1
	v_bfe_i32 v40, v39, 11, 1
	v_bitop3_b32 v24, v9, s6, v24 bitop3:0xe4
	v_bitop3_b32 v9, v25, s6, v40 bitop3:0xe4
	v_bfe_i32 v25, v38, 16, 1
	v_bfe_i32 v40, v39, 16, 1
	v_bitop3_b32 v25, v10, s6, v25 bitop3:0xe4
	v_bitop3_b32 v10, v26, s6, v40 bitop3:0xe4
	v_bfe_i32 v26, v38, 17, 1
	v_bfe_i32 v40, v39, 17, 1
	v_bitop3_b32 v26, v11, s6, v26 bitop3:0xe4
	v_bitop3_b32 v11, v27, s6, v40 bitop3:0xe4
	v_bfe_i32 v27, v38, 18, 1
	v_bfe_i32 v40, v39, 18, 1
	v_bitop3_b32 v27, v12, s6, v27 bitop3:0xe4
	v_bitop3_b32 v12, v28, s6, v40 bitop3:0xe4
	v_bfe_i32 v28, v38, 19, 1
	v_bfe_i32 v40, v39, 19, 1
	v_bitop3_b32 v28, v13, s6, v28 bitop3:0xe4
	v_bitop3_b32 v13, v29, s6, v40 bitop3:0xe4
	v_bfe_i32 v29, v38, 24, 1
	v_bfe_i32 v40, v39, 24, 1
	v_bitop3_b32 v29, v14, s6, v29 bitop3:0xe4
	v_bitop3_b32 v14, v30, s6, v40 bitop3:0xe4
	v_bfe_i32 v30, v38, 25, 1
	v_bfe_i32 v40, v39, 25, 1
	v_bitop3_b32 v30, v15, s6, v30 bitop3:0xe4
	v_bitop3_b32 v15, v31, s6, v40 bitop3:0xe4
	v_bfe_i32 v31, v38, 26, 1
	v_bfe_i32 v40, v39, 26, 1
	v_bitop3_b32 v31, v16, s6, v31 bitop3:0xe4
	v_bitop3_b32 v16, v32, s6, v40 bitop3:0xe4
	v_bfe_i32 v32, v38, 27, 1
	v_bfe_i32 v38, v39, 27, 1
	v_bitop3_b32 v32, v17, s6, v32 bitop3:0xe4
	v_bitop3_b32 v17, v33, s6, v38 bitop3:0xe4
	s_cbranch_vccz .LBB0_1074
	v_max3_f32 v33, v37, v18, v2
	v_max3_f32 v38, v19, v20, v3
	s_nop 0
	v_max3_f32 v33, v33, v4, v5
	v_max3_f32 v38, v38, v23, v24
	s_nop 0
	v_max3_f32 v33, v33, v21, v22
	v_max3_f32 v38, v38, v8, v9
	s_nop 0
	v_max3_f32 v33, v33, v6, v7
	v_max3_f32 v38, v38, v27, v28
	s_nop 0
	v_max3_f32 v33, v33, v25, v26
	v_max3_f32 v38, v38, v12, v13
	s_nop 0
	v_max3_f32 v33, v33, v10, v11
	v_max3_f32 v38, v38, v31, v32
	s_nop 0
	v_max3_f32 v33, v33, v29, v30
	v_max3_f32 v38, v38, v16, v17
	s_nop 0
	v_max3_f32 v33, v33, v14, v15
	s_nop 0
	v_max_f32_e32 v33, v33, v38
	s_nop 0
	v_mov_b32_e32 v38, v33
	s_nop 1
	v_permlane32_swap_b32_e32 v33, v38
	v_max_f32_e32 v33, v33, v38
	s_nop 0
	v_cmp_neq_f32_e32 vcc, s6, v33
	s_nop 1
	v_cndmask_b32_e32 v33, 0, v33, vcc
	v_add_f32_e32 v207, v1, v33
	v_sub_f32_e32 v37, v37, v33
	v_sub_f32_e32 v2, v2, v33
	v_sub_f32_e32 v18, v18, v33
	v_sub_f32_e32 v3, v3, v33
	v_sub_f32_e32 v19, v19, v33
	v_sub_f32_e32 v4, v4, v33
	v_sub_f32_e32 v20, v20, v33
	v_sub_f32_e32 v5, v5, v33
	v_sub_f32_e32 v21, v21, v33
	v_sub_f32_e32 v6, v6, v33
	v_sub_f32_e32 v22, v22, v33
	v_sub_f32_e32 v7, v7, v33
	v_sub_f32_e32 v23, v23, v33
	v_sub_f32_e32 v8, v8, v33
	v_sub_f32_e32 v24, v24, v33
	v_sub_f32_e32 v9, v9, v33
	v_sub_f32_e32 v25, v25, v33
	v_sub_f32_e32 v10, v10, v33
	v_sub_f32_e32 v26, v26, v33
	v_sub_f32_e32 v11, v11, v33
	v_sub_f32_e32 v27, v27, v33
	v_sub_f32_e32 v12, v12, v33
	v_sub_f32_e32 v28, v28, v33
	v_sub_f32_e32 v13, v13, v33
	v_sub_f32_e32 v29, v29, v33
	v_sub_f32_e32 v14, v14, v33
	v_sub_f32_e32 v30, v30, v33
	v_sub_f32_e32 v15, v15, v33
	v_sub_f32_e32 v31, v31, v33
	v_sub_f32_e32 v16, v16, v33
	v_sub_f32_e32 v32, v32, v33
	v_sub_f32_e32 v17, v17, v33
	s_branch .LBB0_1075
